# P5 attention-combine loop: all 16 row loads issued before the first wait (second batch had no dependence on the first)
# baseline (speedup 1.0000x reference)
; __device__ __forceinline__ float bflo(unsigned w) { return __uint_as_float(w << 16); }
; __device__ __forceinline__ float bfhi(unsigned w) { return __uint_as_float(w & 0xffff0000u); }
; __global__ void __launch_bounds__(NTHREADS, 2) hybrid_fwd(Args a) {
;     ...
;                 for (int row0 = gw; row0 < MTOK; row0 += 2 * NGW) {
;                     f32x4 p0[2][4], p1[2][4];
; #pragma unroll
;                     for (int rr = 0; rr < 2; ++rr)
; #pragma unroll
;                         for (int h = 0; h < 4; ++h) { const int row = row0 + rr * NGW; const size_t off = (size_t)(row < MTOK ? row : row0) * 1024 + h * 256 + lane * 4;
;                             const u32x2 a0 = *(const u32x2*)(O0 + off), a1 = *(const u32x2*)(O1 + off);
;                             p0[rr][h] = (f32x4){bflo(a0.x), bfhi(a0.x), bflo(a0.y), bfhi(a0.y)}; p1[rr][h] = (f32x4){bflo(a1.x), bfhi(a1.x), bflo(a1.y), bfhi(a1.y)}; }
.LBB0_750:
	s_add_i32 s10, s79, s4
	s_cmpk_lt_i32 s10, 0x2000
	s_cselect_b32 s12, s10, s4
	s_ashr_i32 s13, s12, 31
	s_ashr_i32 s5, s4, 31
	s_lshl_b64 s[14:15], s[12:13], 11
	s_lshl_b64 s[12:13], s[4:5], 11
	v_or_b32_e32 v38, s12, v1
	v_or_b32_e32 v56, 0x600, v38
	v_mov_b32_e32 v57, s13
	v_lshl_add_u64 v[30:31], s[8:9], 0, v[56:57]
	v_lshl_add_u64 v[34:35], s[6:7], 0, v[56:57]
	v_or_b32_e32 v56, 0x400, v38
	v_lshl_add_u64 v[40:41], s[8:9], 0, v[56:57]
	v_lshl_add_u64 v[44:45], s[6:7], 0, v[56:57]
	v_or_b32_e32 v56, 0x200, v38
	v_lshl_add_u64 v[48:49], s[8:9], 0, v[56:57]
	flat_load_dwordx2 v[46:47], v[44:45]
	flat_load_dwordx2 v[50:51], v[48:49]
	v_mov_b32_e32 v39, s13
	flat_load_dwordx2 v[32:33], v[30:31]
	flat_load_dwordx2 v[36:37], v[34:35]
	flat_load_dwordx2 v[42:43], v[40:41]
	v_xor_b32_e32 v13, 0x80000000, v3
	v_or_b32_e32 v28, s14, v1
	v_mov_b32_e32 v29, s15
	v_lshl_add_u64 v[14:15], s[6:7], 0, v[28:29]
	v_lshl_add_u64 v[16:17], s[8:9], 0, v[28:29]
	v_or_b32_e32 v20, 0x200, v28
	v_mov_b32_e32 v21, s15
	v_or_b32_e32 v24, 0x400, v28
	v_mov_b32_e32 v25, s15
	v_or_b32_e32 v28, 0x600, v28
	v_lshl_add_u64 v[18:19], s[6:7], 0, v[20:21]
	v_lshl_add_u64 v[20:21], s[8:9], 0, v[20:21]
	v_lshl_add_u64 v[22:23], s[6:7], 0, v[24:25]
	v_lshl_add_u64 v[24:25], s[8:9], 0, v[24:25]
	v_lshl_add_u64 v[26:27], s[6:7], 0, v[28:29]
	v_lshl_add_u64 v[28:29], s[8:9], 0, v[28:29]
	flat_load_dwordx2 v[14:15], v[14:15]
	s_cmpk_gt_i32 s10, 0x1fff
	flat_load_dwordx2 v[16:17], v[16:17]
	v_lshl_add_u64 v[168:169], s[6:7], 0, v[56:57]
	v_lshl_add_u64 v[170:171], s[8:9], 0, v[38:39]
	v_lshl_add_u64 v[172:173], s[6:7], 0, v[38:39]
	flat_load_dwordx2 v[54:55], v[168:169]
	flat_load_dwordx2 v[58:59], v[170:171]
	flat_load_dwordx2 v[18:19], v[18:19]
	flat_load_dwordx2 v[20:21], v[20:21]
	flat_load_dwordx2 v[22:23], v[22:23]
	flat_load_dwordx2 v[24:25], v[24:25]
	flat_load_dwordx2 v[26:27], v[26:27]
	flat_load_dwordx2 v[28:29], v[28:29]
	flat_load_dwordx2 v[38:39], v[172:173]
	s_waitcnt vmcnt(0) lgkmcnt(0)
	v_lshlrev_b32_e32 v44, 16, v46
	v_lshlrev_b32_e32 v48, 16, v50
	v_and_b32_e32 v49, 0xffff0000, v50
	v_lshlrev_b32_e32 v52, 16, v51
	v_and_b32_e32 v53, 0xffff0000, v51
	v_and_b32_e32 v45, 0xffff0000, v46
	v_lshlrev_b32_e32 v40, 16, v42
	v_and_b32_e32 v41, 0xffff0000, v42
	v_lshlrev_b32_e32 v42, 16, v43
	v_and_b32_e32 v43, 0xffff0000, v43
	v_lshlrev_b32_e32 v46, 16, v47
	v_and_b32_e32 v47, 0xffff0000, v47
	v_pk_fma_f32 v[42:43], v[12:13], v[42:43], v[46:47]
	v_pk_fma_f32 v[40:41], v[8:9], v[40:41], v[44:45] neg_lo:[1,0,0] neg_hi:[1,0,0]
	v_mul_f32_e32 v44, v43, v43
	v_fmac_f32_e32 v44, v42, v42
	v_lshlrev_b32_e32 v30, 16, v32
	v_and_b32_e32 v31, 0xffff0000, v32
	v_lshlrev_b32_e32 v32, 16, v33
	v_and_b32_e32 v33, 0xffff0000, v33
	v_lshlrev_b32_e32 v34, 16, v36
	v_and_b32_e32 v35, 0xffff0000, v36
	v_lshlrev_b32_e32 v36, 16, v37
	v_and_b32_e32 v37, 0xffff0000, v37
	v_pk_fma_f32 v[32:33], v[12:13], v[32:33], v[36:37]
	v_pk_fma_f32 v[30:31], v[8:9], v[30:31], v[34:35] neg_lo:[1,0,0] neg_hi:[1,0,0]
	v_mul_f32_e32 v34, v33, v33
	v_fmac_f32_e32 v34, v32, v32
	s_waitcnt vmcnt(0) lgkmcnt(0)
	v_lshlrev_b32_e32 v50, 16, v54
	v_lshlrev_b32_e32 v56, 16, v58
	v_and_b32_e32 v57, 0xffff0000, v58
	v_lshlrev_b32_e32 v58, 16, v59
	v_and_b32_e32 v59, 0xffff0000, v59
	v_lshlrev_b32_e32 v60, 16, v38
	v_and_b32_e32 v61, 0xffff0000, v38
	v_lshlrev_b32_e32 v62, 16, v39
	v_and_b32_e32 v63, 0xffff0000, v39
	v_pk_fma_f32 v[58:59], v[12:13], v[58:59], v[62:63]
	v_pk_fma_f32 v[56:57], v[8:9], v[56:57], v[60:61] neg_lo:[1,0,0] neg_hi:[1,0,0]
	v_mul_f32_e32 v60, v59, v59
	v_mul_f32_e32 v2, v57, v57
	v_fmac_f32_e32 v2, v56, v56
	v_fmac_f32_e32 v60, v58, v58
	v_add_f32_e32 v2, v2, v60
	v_and_b32_e32 v51, 0xffff0000, v54
	v_lshlrev_b32_e32 v54, 16, v55
	v_add_f32_dpp v2, v2, v2 quad_perm:[1,0,3,2] row_mask:0xf bank_mask:0xf bound_ctrl:1
	v_and_b32_e32 v55, 0xffff0000, v55
	v_pk_fma_f32 v[52:53], v[12:13], v[52:53], v[54:55]
	v_add_f32_dpp v2, v2, v2 quad_perm:[2,3,0,1] row_mask:0xf bank_mask:0xf bound_ctrl:1
	v_pk_fma_f32 v[48:49], v[8:9], v[48:49], v[50:51] neg_lo:[1,0,0] neg_hi:[1,0,0]
	v_mul_f32_e32 v50, v53, v53
	v_add_f32_dpp v2, v2, v2 row_ror:4 row_mask:0xf bank_mask:0xf bound_ctrl:1
	v_fmac_f32_e32 v50, v52, v52
	v_lshl_add_u64 v[38:39], v[10:11], 0, s[12:13]
	v_add_f32_dpp v2, v2, v2 row_ror:8 row_mask:0xf bank_mask:0xf bound_ctrl:1
	v_mov_b32_e32 v60, v2
	s_nop 1
	v_permlane16_swap_b32_e32 v2, v60
	v_add_f32_e32 v2, v2, v60
	v_mov_b32_e32 v60, v2
	s_nop 1
	v_permlane32_swap_b32_e32 v2, v60
	v_add_f32_e32 v2, v2, v60
	v_fmamk_f32 v2, v2, 0x3b800000, v207
	v_rsq_f32_e32 v2, v2
	s_nop 0
	v_pk_mul_f32 v[56:57], v[56:57], v[2:3] op_sel_hi:[1,0]
	v_pk_mul_f32 v[58:59], v[58:59], v[2:3] op_sel_hi:[1,0]
	v_pk_mul_f32 v[56:57], v[6:7], v[56:57]
	v_pk_mul_f32 v[58:59], v[4:5], v[58:59]
	v_mul_f32_e32 v2, 4.0, v56
	v_mul_f32_e32 v56, 4.0, v57
	v_mul_f32_e32 v57, 4.0, v58
	v_mul_f32_e32 v58, 4.0, v59
	v_med3_f32 v2, v2, s69, v208
	v_med3_f32 v56, v56, s69, v208
	v_mov_b32_e32 v59, v193
	v_cvt_pk_fp8_f32 v59, v2, v56
	v_mul_f32_e32 v2, v49, v49
	v_fmac_f32_e32 v2, v48, v48
	v_add_f32_e32 v2, v2, v50
	v_med3_f32 v57, v57, s69, v208
	v_med3_f32 v58, v58, s69, v208
	v_add_f32_dpp v2, v2, v2 quad_perm:[1,0,3,2] row_mask:0xf bank_mask:0xf bound_ctrl:1
	v_cvt_pk_fp8_f32 v59, v57, v58 op_sel:[0,0,1]
	flat_store_dword v[38:39], v59 nt
	v_add_f32_dpp v2, v2, v2 quad_perm:[2,3,0,1] row_mask:0xf bank_mask:0xf bound_ctrl:1
	s_nop 1
	v_add_f32_dpp v2, v2, v2 row_ror:4 row_mask:0xf bank_mask:0xf bound_ctrl:1
	s_nop 1
	v_add_f32_dpp v2, v2, v2 row_ror:8 row_mask:0xf bank_mask:0xf bound_ctrl:1
	v_mov_b32_e32 v50, v2
; __global__ void __launch_bounds__(NTHREADS, 2) hybrid_fwd(Args a) {
;     ...
;                     for (int rr = 0; rr < 2; ++rr) { const int row = row0 + rr * NGW;
;                         if (row < MTOK) {
; #pragma unroll
;                             for (int h = 0; h < 4; ++h) {
;                                 const f32x4 o = p0[rr][h] - p1[rr][h] * lam;
;                                 const float ss = wave_sum((o[0] * o[0] + o[1] * o[1]) + (o[2] * o[2] + o[3] * o[3]));
;                                 const float r = __builtin_amdgcn_rsqf(ss * (1.f / 256.f) + LN_EPS);
;                                 const f32x4 y = o * r * sg;
;                                 __builtin_nontemporal_store(cvt4_fp8(y[0] * CAT_SCALE, y[1] * CAT_SCALE, y[2] * CAT_SCALE, y[3] * CAT_SCALE), (unsigned*)(CAT + (size_t)row * DM + h * 256 + lane * 4)); } } }
	s_nop 1
	v_permlane16_swap_b32_e32 v2, v50
	v_add_f32_e32 v2, v2, v50
	v_mov_b32_e32 v50, v2
	s_nop 1
	v_permlane32_swap_b32_e32 v2, v50
	v_add_f32_e32 v2, v2, v50
	v_fmamk_f32 v2, v2, 0x3b800000, v207
	v_rsq_f32_e32 v2, v2
	s_nop 0
	v_pk_mul_f32 v[48:49], v[48:49], v[2:3] op_sel_hi:[1,0]
	v_pk_mul_f32 v[50:51], v[52:53], v[2:3] op_sel_hi:[1,0]
	v_pk_mul_f32 v[48:49], v[6:7], v[48:49]
	v_pk_mul_f32 v[50:51], v[4:5], v[50:51]
	v_mul_f32_e32 v2, 4.0, v48
	v_mul_f32_e32 v48, 4.0, v49
	v_mul_f32_e32 v49, 4.0, v50
	v_mul_f32_e32 v50, 4.0, v51
	v_med3_f32 v2, v2, s69, v208
	v_med3_f32 v48, v48, s69, v208
	v_mov_b32_e32 v51, v193
	v_cvt_pk_fp8_f32 v51, v2, v48
	v_mul_f32_e32 v2, v41, v41
	v_fmac_f32_e32 v2, v40, v40
	v_add_f32_e32 v2, v2, v44
	v_med3_f32 v49, v49, s69, v208
	v_med3_f32 v50, v50, s69, v208
	v_add_f32_dpp v2, v2, v2 quad_perm:[1,0,3,2] row_mask:0xf bank_mask:0xf bound_ctrl:1
	v_cvt_pk_fp8_f32 v51, v49, v50 op_sel:[0,0,1]
	flat_store_dword v[38:39], v51 offset:256 nt
	v_add_f32_dpp v2, v2, v2 quad_perm:[2,3,0,1] row_mask:0xf bank_mask:0xf bound_ctrl:1
	s_nop 1
	v_add_f32_dpp v2, v2, v2 row_ror:4 row_mask:0xf bank_mask:0xf bound_ctrl:1
	s_nop 1
	v_add_f32_dpp v2, v2, v2 row_ror:8 row_mask:0xf bank_mask:0xf bound_ctrl:1
	v_mov_b32_e32 v44, v2
	s_nop 1
	v_permlane16_swap_b32_e32 v2, v44
	v_add_f32_e32 v2, v2, v44
	v_mov_b32_e32 v44, v2
	s_nop 1
	v_permlane32_swap_b32_e32 v2, v44
	v_add_f32_e32 v2, v2, v44
	v_fmamk_f32 v2, v2, 0x3b800000, v207
	v_rsq_f32_e32 v2, v2
	s_nop 0
	v_pk_mul_f32 v[40:41], v[40:41], v[2:3] op_sel_hi:[1,0]
	v_pk_mul_f32 v[42:43], v[42:43], v[2:3] op_sel_hi:[1,0]
	v_pk_mul_f32 v[40:41], v[6:7], v[40:41]
	v_pk_mul_f32 v[42:43], v[4:5], v[42:43]
	v_mul_f32_e32 v2, 4.0, v40
	v_mul_f32_e32 v40, 4.0, v41
	v_mul_f32_e32 v41, 4.0, v42
	v_mul_f32_e32 v42, 4.0, v43
	v_med3_f32 v2, v2, s69, v208
	v_med3_f32 v40, v40, s69, v208
	v_mov_b32_e32 v43, v193
	v_cvt_pk_fp8_f32 v43, v2, v40
	v_mul_f32_e32 v2, v31, v31
	v_fmac_f32_e32 v2, v30, v30
	v_add_f32_e32 v2, v2, v34
	v_med3_f32 v41, v41, s69, v208
	v_med3_f32 v42, v42, s69, v208
	v_add_f32_dpp v2, v2, v2 quad_perm:[1,0,3,2] row_mask:0xf bank_mask:0xf bound_ctrl:1
	v_cvt_pk_fp8_f32 v43, v41, v42 op_sel:[0,0,1]
	flat_store_dword v[38:39], v43 offset:512 nt
	v_add_f32_dpp v2, v2, v2 quad_perm:[2,3,0,1] row_mask:0xf bank_mask:0xf bound_ctrl:1
	s_nop 1
	v_add_f32_dpp v2, v2, v2 row_ror:4 row_mask:0xf bank_mask:0xf bound_ctrl:1
	s_nop 1
	v_add_f32_dpp v2, v2, v2 row_ror:8 row_mask:0xf bank_mask:0xf bound_ctrl:1
	v_mov_b32_e32 v34, v2
	s_nop 1
	v_permlane16_swap_b32_e32 v2, v34
	v_add_f32_e32 v2, v2, v34
	v_mov_b32_e32 v34, v2
	s_nop 1
	v_permlane32_swap_b32_e32 v2, v34
	v_add_f32_e32 v2, v2, v34
	v_fmamk_f32 v2, v2, 0x3b800000, v207
	v_rsq_f32_e32 v2, v2
	s_nop 0
	v_pk_mul_f32 v[30:31], v[30:31], v[2:3] op_sel_hi:[1,0]
	v_pk_mul_f32 v[32:33], v[32:33], v[2:3] op_sel_hi:[1,0]
	v_pk_mul_f32 v[30:31], v[6:7], v[30:31]
	v_pk_mul_f32 v[32:33], v[4:5], v[32:33]
	v_mul_f32_e32 v2, 4.0, v30
	v_mul_f32_e32 v30, 4.0, v31
	v_mul_f32_e32 v31, 4.0, v32
	v_mul_f32_e32 v32, 4.0, v33
	v_med3_f32 v2, v2, s69, v208
	v_med3_f32 v30, v30, s69, v208
	v_mov_b32_e32 v33, v193
	v_cvt_pk_fp8_f32 v33, v2, v30
	v_med3_f32 v31, v31, s69, v208
	v_med3_f32 v32, v32, s69, v208
	v_cvt_pk_fp8_f32 v33, v31, v32 op_sel:[0,0,1]
	flat_store_dword v[38:39], v33 offset:768 nt
	s_cbranch_scc1 .LBB0_749
; __global__ void __launch_bounds__(NTHREADS, 2) hybrid_fwd(Args a) {
;     ...
;                     for (int rr = 0; rr < 2; ++rr) { const int row = row0 + rr * NGW;
;                         if (row < MTOK) {
; #pragma unroll
;                             for (int h = 0; h < 4; ++h) {
;                                 const f32x4 o = p0[rr][h] - p1[rr][h] * lam;
;                                 const float ss = wave_sum((o[0] * o[0] + o[1] * o[1]) + (o[2] * o[2] + o[3] * o[3]));
;                                 const float r = __builtin_amdgcn_rsqf(ss * (1.f / 256.f) + LN_EPS);
;                                 const f32x4 y = o * r * sg;
;                                 __builtin_nontemporal_store(cvt4_fp8(y[0] * CAT_SCALE, y[1] * CAT_SCALE, y[2] * CAT_SCALE, y[3] * CAT_SCALE), (unsigned*)(CAT + (size_t)row * DM + h * 256 + lane * 4)); } } }
	v_lshlrev_b32_e32 v42, 16, v16
	v_and_b32_e32 v43, 0xffff0000, v16
	v_lshlrev_b32_e32 v16, 16, v17
	v_and_b32_e32 v17, 0xffff0000, v17
	v_lshlrev_b32_e32 v44, 16, v14
	v_and_b32_e32 v45, 0xffff0000, v14
	v_lshlrev_b32_e32 v14, 16, v15
	v_and_b32_e32 v15, 0xffff0000, v15
	v_pk_fma_f32 v[14:15], v[12:13], v[16:17], v[14:15]
	v_pk_fma_f32 v[16:17], v[8:9], v[42:43], v[44:45] neg_lo:[1,0,0] neg_hi:[1,0,0]
	v_mul_f32_e32 v42, v15, v15
	v_mul_f32_e32 v2, v17, v17
	v_fmac_f32_e32 v2, v16, v16
	v_fmac_f32_e32 v42, v14, v14
	v_add_f32_e32 v2, v2, v42
	v_lshlrev_b32_e32 v38, 16, v20
	v_and_b32_e32 v39, 0xffff0000, v20
	v_add_f32_dpp v2, v2, v2 quad_perm:[1,0,3,2] row_mask:0xf bank_mask:0xf bound_ctrl:1
	v_lshlrev_b32_e32 v20, 16, v21
	v_and_b32_e32 v21, 0xffff0000, v21
	v_add_f32_dpp v2, v2, v2 quad_perm:[2,3,0,1] row_mask:0xf bank_mask:0xf bound_ctrl:1
	v_lshlrev_b32_e32 v40, 16, v18
	v_and_b32_e32 v41, 0xffff0000, v18
	v_add_f32_dpp v2, v2, v2 row_ror:4 row_mask:0xf bank_mask:0xf bound_ctrl:1
	v_lshlrev_b32_e32 v18, 16, v19
	v_and_b32_e32 v19, 0xffff0000, v19
	v_add_f32_dpp v2, v2, v2 row_ror:8 row_mask:0xf bank_mask:0xf bound_ctrl:1
	v_mov_b32_e32 v42, v2
	s_nop 1
	v_permlane16_swap_b32_e32 v2, v42
	v_add_f32_e32 v2, v2, v42
	v_mov_b32_e32 v42, v2
	s_nop 1
	v_permlane32_swap_b32_e32 v2, v42
	v_add_f32_e32 v2, v2, v42
	v_fmamk_f32 v2, v2, 0x3b800000, v207
	v_rsq_f32_e32 v2, v2
	v_mov_b32_e32 v46, v193
	v_lshlrev_b32_e32 v34, 16, v24
	v_and_b32_e32 v35, 0xffff0000, v24
	v_pk_mul_f32 v[16:17], v[16:17], v[2:3] op_sel_hi:[1,0]
	v_pk_mul_f32 v[14:15], v[14:15], v[2:3] op_sel_hi:[1,0]
	v_pk_mul_f32 v[16:17], v[6:7], v[16:17]
	v_pk_mul_f32 v[14:15], v[4:5], v[14:15]
	v_mul_f32_e32 v2, 4.0, v16
	v_mul_f32_e32 v16, 4.0, v17
	v_mul_f32_e32 v44, 4.0, v14
	v_med3_f32 v2, v2, s69, v208
	v_med3_f32 v14, v16, s69, v208
	v_mul_f32_e32 v45, 4.0, v15
	v_cvt_pk_fp8_f32 v46, v2, v14
	v_pk_fma_f32 v[14:15], v[12:13], v[20:21], v[18:19]
	v_pk_fma_f32 v[16:17], v[8:9], v[38:39], v[40:41] neg_lo:[1,0,0] neg_hi:[1,0,0]
	v_mul_f32_e32 v18, v15, v15
	v_mul_f32_e32 v2, v17, v17
	v_fmac_f32_e32 v2, v16, v16
	v_fmac_f32_e32 v18, v14, v14
	v_add_f32_e32 v2, v2, v18
	v_med3_f32 v19, v45, s69, v208
	v_lshlrev_b32_e32 v24, 16, v25
	v_add_f32_dpp v2, v2, v2 quad_perm:[1,0,3,2] row_mask:0xf bank_mask:0xf bound_ctrl:1
	v_and_b32_e32 v25, 0xffff0000, v25
	v_lshlrev_b32_e32 v36, 16, v22
	v_add_f32_dpp v2, v2, v2 quad_perm:[2,3,0,1] row_mask:0xf bank_mask:0xf bound_ctrl:1
	v_and_b32_e32 v37, 0xffff0000, v22
	v_lshlrev_b32_e32 v22, 16, v23
	v_add_f32_dpp v2, v2, v2 row_ror:4 row_mask:0xf bank_mask:0xf bound_ctrl:1
	v_and_b32_e32 v23, 0xffff0000, v23
	v_mov_b32_e32 v20, v193
	v_add_f32_dpp v2, v2, v2 row_ror:8 row_mask:0xf bank_mask:0xf bound_ctrl:1
	v_mov_b32_e32 v18, v2
	s_nop 1
	v_permlane16_swap_b32_e32 v2, v18
	v_add_f32_e32 v2, v2, v18
	v_mov_b32_e32 v18, v2
	s_nop 1
	v_permlane32_swap_b32_e32 v2, v18
	v_add_f32_e32 v2, v2, v18
	v_fmamk_f32 v2, v2, 0x3b800000, v207
	v_rsq_f32_e32 v2, v2
	v_med3_f32 v18, v44, s69, v208
	v_cvt_pk_fp8_f32 v46, v18, v19 op_sel:[0,0,1]
	v_lshlrev_b32_e32 v30, 16, v28
	v_pk_mul_f32 v[16:17], v[16:17], v[2:3] op_sel_hi:[1,0]
	v_pk_mul_f32 v[14:15], v[14:15], v[2:3] op_sel_hi:[1,0]
	v_pk_mul_f32 v[16:17], v[6:7], v[16:17]
	v_pk_mul_f32 v[14:15], v[4:5], v[14:15]
	v_mul_f32_e32 v2, 4.0, v16
	v_mul_f32_e32 v16, 4.0, v17
	v_mul_f32_e32 v18, 4.0, v14
	v_med3_f32 v2, v2, s69, v208
	v_med3_f32 v14, v16, s69, v208
	v_mul_f32_e32 v19, 4.0, v15
	v_cvt_pk_fp8_f32 v20, v2, v14
	v_pk_fma_f32 v[14:15], v[12:13], v[24:25], v[22:23]
	v_pk_fma_f32 v[16:17], v[8:9], v[34:35], v[36:37] neg_lo:[1,0,0] neg_hi:[1,0,0]
	v_mul_f32_e32 v21, v15, v15
	v_mul_f32_e32 v2, v17, v17
	v_fmac_f32_e32 v2, v16, v16
	v_fmac_f32_e32 v21, v14, v14
	v_add_f32_e32 v2, v2, v21
	v_med3_f32 v18, v18, s69, v208
	v_med3_f32 v19, v19, s69, v208
	v_add_f32_dpp v2, v2, v2 quad_perm:[1,0,3,2] row_mask:0xf bank_mask:0xf bound_ctrl:1
	v_and_b32_e32 v31, 0xffff0000, v28
	v_lshlrev_b32_e32 v28, 16, v29
	v_add_f32_dpp v2, v2, v2 quad_perm:[2,3,0,1] row_mask:0xf bank_mask:0xf bound_ctrl:1
	v_and_b32_e32 v29, 0xffff0000, v29
	v_lshlrev_b32_e32 v32, 16, v26
	v_add_f32_dpp v2, v2, v2 row_ror:4 row_mask:0xf bank_mask:0xf bound_ctrl:1
	v_and_b32_e32 v33, 0xffff0000, v26
	v_lshlrev_b32_e32 v26, 16, v27
	v_add_f32_dpp v2, v2, v2 row_ror:8 row_mask:0xf bank_mask:0xf bound_ctrl:1
	v_mov_b32_e32 v21, v2
	s_nop 1
	v_permlane16_swap_b32_e32 v2, v21
	v_add_f32_e32 v2, v2, v21
	v_mov_b32_e32 v21, v2
	s_nop 1
	v_permlane32_swap_b32_e32 v2, v21
	v_add_f32_e32 v2, v2, v21
	v_fmamk_f32 v2, v2, 0x3b800000, v207
	v_rsq_f32_e32 v2, v2
	v_and_b32_e32 v27, 0xffff0000, v27
	v_cvt_pk_fp8_f32 v20, v18, v19 op_sel:[0,0,1]
	v_mov_b32_e32 v21, v193
	v_pk_mul_f32 v[16:17], v[16:17], v[2:3] op_sel_hi:[1,0]
	v_pk_mul_f32 v[14:15], v[14:15], v[2:3] op_sel_hi:[1,0]
	v_pk_mul_f32 v[16:17], v[6:7], v[16:17]
	v_pk_mul_f32 v[14:15], v[4:5], v[14:15]
	v_mul_f32_e32 v2, 4.0, v16
	v_mul_f32_e32 v16, 4.0, v17
	v_mul_f32_e32 v18, 4.0, v14
	v_med3_f32 v2, v2, s69, v208
	v_med3_f32 v14, v16, s69, v208
	v_mul_f32_e32 v19, 4.0, v15
	v_cvt_pk_fp8_f32 v21, v2, v14
	v_pk_fma_f32 v[14:15], v[12:13], v[28:29], v[26:27]
	v_pk_fma_f32 v[16:17], v[8:9], v[30:31], v[32:33] neg_lo:[1,0,0] neg_hi:[1,0,0]
	v_mul_f32_e32 v13, v15, v15
	v_mul_f32_e32 v2, v17, v17
	v_fmac_f32_e32 v2, v16, v16
	v_fmac_f32_e32 v13, v14, v14
	v_add_f32_e32 v2, v2, v13
	s_ashr_i32 s11, s10, 31
	s_lshl_b64 s[10:11], s[10:11], 11
	v_add_f32_dpp v2, v2, v2 quad_perm:[1,0,3,2] row_mask:0xf bank_mask:0xf bound_ctrl:1
	v_lshl_add_u64 v[42:43], v[10:11], 0, s[10:11]
	s_nop 0
	v_add_f32_dpp v2, v2, v2 quad_perm:[2,3,0,1] row_mask:0xf bank_mask:0xf bound_ctrl:1
	s_nop 1
	v_add_f32_dpp v2, v2, v2 row_ror:4 row_mask:0xf bank_mask:0xf bound_ctrl:1
	s_nop 1
	v_add_f32_dpp v2, v2, v2 row_ror:8 row_mask:0xf bank_mask:0xf bound_ctrl:1
	v_mov_b32_e32 v13, v2
	s_nop 1
	v_permlane16_swap_b32_e32 v2, v13
	v_add_f32_e32 v2, v2, v13
	v_mov_b32_e32 v13, v2
	s_nop 1
	v_permlane32_swap_b32_e32 v2, v13
	v_add_f32_e32 v2, v2, v13
	v_fmamk_f32 v2, v2, 0x3b800000, v207
	v_rsq_f32_e32 v2, v2
	v_med3_f32 v13, v18, s69, v208
	v_med3_f32 v18, v19, s69, v208
	v_cvt_pk_fp8_f32 v21, v13, v18 op_sel:[0,0,1]
	v_pk_mul_f32 v[16:17], v[16:17], v[2:3] op_sel_hi:[1,0]
	v_pk_mul_f32 v[14:15], v[14:15], v[2:3] op_sel_hi:[1,0]
	v_pk_mul_f32 v[16:17], v[6:7], v[16:17]
	v_pk_mul_f32 v[14:15], v[4:5], v[14:15]
	v_mul_f32_e32 v2, 4.0, v16
	v_mul_f32_e32 v13, 4.0, v17
	v_med3_f32 v2, v2, s69, v208
	v_med3_f32 v13, v13, s69, v208
	v_mov_b32_e32 v16, v193
	v_cvt_pk_fp8_f32 v16, v2, v13
	v_mul_f32_e32 v14, 4.0, v14
	v_mul_f32_e32 v2, 4.0, v15
	v_med3_f32 v13, v14, s69, v208
	v_med3_f32 v2, v2, s69, v208
	v_cvt_pk_fp8_f32 v16, v13, v2 op_sel:[0,0,1]
	flat_store_dword v[42:43], v46 nt
	flat_store_dword v[42:43], v20 offset:256 nt
	flat_store_dword v[42:43], v21 offset:512 nt
	flat_store_dword v[42:43], v16 offset:768 nt
	s_branch .LBB0_749
